# GEMM_A block mapping rebalanced: self-projection panels get 28 chunks of 23 row-groups (56 blocks), quant panels keep 25x25; 256 active blocks, 32 per XCD
# speedup vs baseline: 1.1170x; 1.0007x over previous
_Z6gemm_kILi0ELi1ELi2EEvPKDF16_S1_iiiPKfS1_PDF16_PfS4_:
	s_lshr_b32 s37, s2, 3
	s_cmp_lt_u32 s37, 128
	s_cbranch_scc1 LgA_exit
	s_sub_u32 s37, s37, 128
	s_and_b32 s36, s2, 7
	s_cmp_ge_u32 s37, 25
	s_cbranch_scc1 LgA_map_self
	s_lshr_b32 s38, s37, 3
	s_and_b32 s21, s37, 7
	s_mul_i32 s39, s36, 3
	s_add_u32 s22, s39, s38
	s_cmp_eq_u32 s37, 24
	s_cselect_b32 s22, 24, s22
	s_cselect_b32 s21, s36, s21
	s_mul_i32 s23, s22, 25
	s_mov_b32 s24, 25
	s_branch LgA_map_done
LgA_map_self:
	s_mul_i32 s38, s36, 7
	s_add_u32 s38, s38, s37
	s_sub_u32 s38, s38, 25
	s_lshr_b32 s22, s38, 1
	s_and_b32 s21, s38, 1
	s_add_u32 s21, s21, 8
	s_mul_i32 s23, s22, 23
	s_sub_u32 s24, 625, s23
	s_min_u32 s24, s24, 23
LgA_map_done:
	s_load_dwordx4 s[4:7], s[0:1], 0x0
	s_load_dwordx4 s[8:11], s[0:1], 0x20
	s_load_dwordx4 s[12:15], s[0:1], 0x30
	s_load_dwordx2 s[16:17], s[0:1], 0x40
	v_lshrrev_b32_e32 v20, 6, v0
	v_and_b32_e32 v1, 63, v0
	v_readfirstlane_b32 s20, v20
	v_and_b32_e32 v2, 15, v0
	v_bfe_u32 v3, v0, 4, 2
	v_and_b32_e32 v16, 7, v2
	v_xor_b32_e32 v16, v16, v3
	v_lshlrev_b32_e32 v16, 4, v16
	v_lshl_or_b32 v4, v2, 7, v16
	v_lshrrev_b32_e32 v16, 3, v1
	v_and_b32_e32 v17, 7, v1
	v_xor_b32_e32 v17, v17, v16
	v_lshlrev_b32_e32 v17, 4, v17
	v_lshl_or_b32 v9, v16, 7, v17
	v_add_u32_e32 v10, 0x140000, v9
	s_waitcnt lgkmcnt(0)
	s_mul_i32 s36, s20, 0x280000
	s_lshl_b32 s37, s23, 11
	s_add_u32 s36, s36, s37
	s_add_u32 s26, s4, s36
	s_addc_u32 s27, s5, 0
	s_mul_i32 s28, s20, 0x1000
	s_add_u32 s46, s28, 0x14000
	s_mov_b32 s47, s28
	s_mov_b32 s29, 0
	s_cmp_ge_u32 s21, 8
	s_cbranch_scc1 LgA_setup_self
	v_mul_u32_u24_e32 v16, 2176, v2
	v_lshl_add_u32 v14, v3, 4, v16
	s_lshr_b32 s36, s21, 1
	s_lshl_b32 s37, s23, 6
	s_add_u32 s36, s36, s37
	s_mul_i32 s36, s36, 544
	s_and_b32 s37, s21, 1
	s_lshl_b32 s38, s37, 8
	s_lshl_b32 s39, s20, 6
	s_add_u32 s38, s38, s39
	s_add_u32 s36, s36, s38
	s_add_u32 s30, s12, s36
	s_addc_u32 s31, s13, 0
	s_mul_i32 s37, s37, 240
	s_mul_i32 s39, s20, 60
	s_add_u32 s37, s37, s39
	s_sub_u32 s37, 512, s37
	v_add_u32_e32 v112, s37, v16
	s_mov_b32 s44, 0x0c0c0400
	s_mov_b32 s45, 0x05040100
	s_branch LgA_setup_done

	.amdhsa_kernel _Z6gemm_kILi0ELi1ELi2EEvPKDF16_S1_iiiPKfS1_PDF16_PfS4_
		.amdhsa_group_segment_fixed_size 81920
		.amdhsa_private_segment_fixed_size 0
		.amdhsa_kernarg_size 72
		.amdhsa_user_sgpr_count 2
		.amdhsa_user_sgpr_dispatch_ptr 0
		.amdhsa_user_sgpr_queue_ptr 0
		.amdhsa_user_sgpr_kernarg_segment_ptr 1
		.amdhsa_user_sgpr_dispatch_id 0
		.amdhsa_user_sgpr_kernarg_preload_length 0
		.amdhsa_user_sgpr_kernarg_preload_offset 0
		.amdhsa_user_sgpr_private_segment_size 0
		.amdhsa_uses_dynamic_stack 0
		.amdhsa_enable_private_segment 0
		.amdhsa_system_sgpr_workgroup_id_x 1
		.amdhsa_system_sgpr_workgroup_id_y 0
		.amdhsa_system_sgpr_workgroup_id_z 0
		.amdhsa_system_sgpr_workgroup_info 0
		.amdhsa_system_vgpr_workitem_id 0
		.amdhsa_next_free_vgpr 512
		.amdhsa_next_free_sgpr 64
		.amdhsa_accum_offset 256
		.amdhsa_reserve_vcc 1
		.amdhsa_float_round_mode_32 0
		.amdhsa_float_round_mode_16_64 0
		.amdhsa_float_denorm_mode_32 3
		.amdhsa_float_denorm_mode_16_64 3
		.amdhsa_dx10_clamp 1
		.amdhsa_ieee_mode 1
		.amdhsa_fp16_overflow 0
		.amdhsa_tg_split 0
		.amdhsa_exception_fp_ieee_invalid_op 0
		.amdhsa_exception_fp_denorm_src 0
		.amdhsa_exception_fp_ieee_div_zero 0
		.amdhsa_exception_fp_ieee_overflow 0
		.amdhsa_exception_fp_ieee_underflow 0
		.amdhsa_exception_fp_ieee_inexact 0
		.amdhsa_exception_int_div_zero 0
	.end_amdhsa_kernel

amdhsa.kernels:
  - .agpr_count:     0
    .args:
      - .actual_access:  read_only
        .address_space:  global
        .offset:         0
        .size:           8
        .value_kind:     global_buffer
      - .actual_access:  write_only
        .address_space:  global
        .offset:         8
        .size:           8
        .value_kind:     global_buffer
      - .actual_access:  read_only
        .address_space:  global
        .offset:         16
        .size:           8
        .value_kind:     global_buffer
      - .actual_access:  read_only
        .address_space:  global
        .offset:         24
        .size:           8
        .value_kind:     global_buffer
      - .actual_access:  read_only
        .address_space:  global
        .offset:         32
        .size:           8
        .value_kind:     global_buffer
      - .actual_access:  read_only
        .address_space:  global
        .offset:         40
        .size:           8
        .value_kind:     global_buffer
      - .actual_access:  write_only
        .address_space:  global
        .offset:         48
        .size:           8
        .value_kind:     global_buffer
      - .actual_access:  read_only
        .address_space:  global
        .offset:         56
        .size:           8
        .value_kind:     global_buffer
      - .actual_access:  read_only
        .address_space:  global
        .offset:         64
        .size:           8
        .value_kind:     global_buffer
      - .actual_access:  read_only
        .address_space:  global
        .offset:         72
        .size:           8
        .value_kind:     global_buffer
      - .actual_access:  read_only
        .address_space:  global
        .offset:         80
        .size:           8
        .value_kind:     global_buffer
      - .actual_access:  read_only
        .address_space:  global
        .offset:         88
        .size:           8
        .value_kind:     global_buffer
      - .actual_access:  write_only
        .address_space:  global
        .offset:         96
        .size:           8
        .value_kind:     global_buffer
      - .actual_access:  write_only
        .address_space:  global
        .offset:         104
        .size:           8
        .value_kind:     global_buffer
      - .actual_access:  write_only
        .address_space:  global
        .offset:         112
        .size:           8
        .value_kind:     global_buffer
    .group_segment_fixed_size: 51552
    .kernarg_segment_align: 8
    .kernarg_segment_size: 120
    .language:       OpenCL C
    .language_version:
      - 2
      - 0
    .max_flat_workgroup_size: 1024
    .name:           _Z6prep_kPKfPDF16_S0_S0_S0_S0_S1_S1_S1_PKiS3_S3_PiS4_S4_
    .private_segment_fixed_size: 0
    .sgpr_count:     106
    .sgpr_spill_count: 15
    .symbol:         _Z6prep_kPKfPDF16_S0_S0_S0_S0_S1_S1_S1_PKiS3_S3_PiS4_S4_.kd
    .uniform_work_group_size: 1
    .uses_dynamic_stack: false
    .vgpr_count:     48
    .vgpr_spill_count: 0
    .wavefront_size: 64
  - .agpr_count:     0
    .args:
      - .actual_access:  read_only
        .address_space:  global
        .offset:         0
        .size:           8
        .value_kind:     global_buffer
      - .actual_access:  read_only
        .address_space:  global
        .offset:         8
        .size:           8
        .value_kind:     global_buffer
      - .actual_access:  read_only
        .address_space:  global
        .offset:         16
        .size:           8
        .value_kind:     global_buffer
      - .actual_access:  read_only
        .address_space:  global
        .offset:         24
        .size:           8
        .value_kind:     global_buffer
      - .actual_access:  read_only
        .address_space:  global
        .offset:         32
        .size:           8
        .value_kind:     global_buffer
      - .actual_access:  read_only
        .address_space:  global
        .offset:         40
        .size:           8
        .value_kind:     global_buffer
      - .actual_access:  read_only
        .address_space:  global
        .offset:         48
        .size:           8
        .value_kind:     global_buffer
      - .actual_access:  read_only
        .address_space:  global
        .offset:         56
        .size:           8
        .value_kind:     global_buffer
      - .actual_access:  read_only
        .address_space:  global
        .offset:         64
        .size:           8
        .value_kind:     global_buffer
      - .actual_access:  write_only
        .address_space:  global
        .offset:         72
        .size:           8
        .value_kind:     global_buffer
      - .actual_access:  read_only
        .address_space:  global
        .offset:         80
        .size:           8
        .value_kind:     global_buffer
      - .actual_access:  read_only
        .address_space:  global
        .offset:         88
        .size:           8
        .value_kind:     global_buffer
      - .actual_access:  write_only
        .address_space:  global
        .offset:         96
        .size:           8
        .value_kind:     global_buffer
      - .actual_access:  write_only
        .address_space:  global
        .offset:         104
        .size:           8
        .value_kind:     global_buffer
    .group_segment_fixed_size: 16640
    .kernarg_segment_align: 8
    .kernarg_segment_size: 112
    .language:       OpenCL C
    .language_version:
      - 2
      - 0
    .max_flat_workgroup_size: 256
    .name:           _Z7agg_ln1PKDF16_S0_S0_PKiS2_S2_PKfS4_S4_PDF16_S4_S4_S5_S5_
    .private_segment_fixed_size: 0
    .sgpr_count:     45
    .sgpr_spill_count: 0
    .symbol:         _Z7agg_ln1PKDF16_S0_S0_PKiS2_S2_PKfS4_S4_PDF16_S4_S4_S5_S5_.kd
    .uniform_work_group_size: 1
    .uses_dynamic_stack: false
    .vgpr_count:     64
    .vgpr_spill_count: 0
    .wavefront_size: 64
  - .agpr_count:     0
    .args:
      - .actual_access:  read_only
        .address_space:  global
        .offset:         0
        .size:           8
        .value_kind:     global_buffer
      - .actual_access:  read_only
        .address_space:  global
        .offset:         8
        .size:           8
        .value_kind:     global_buffer
      - .actual_access:  read_only
        .address_space:  global
        .offset:         16
        .size:           8
        .value_kind:     global_buffer
      - .actual_access:  write_only
        .address_space:  global
        .offset:         24
        .size:           8
        .value_kind:     global_buffer
    .group_segment_fixed_size: 0
    .kernarg_segment_align: 8
    .kernarg_segment_size: 32
    .language:       OpenCL C
    .language_version:
      - 2
      - 0
    .max_flat_workgroup_size: 256
    .name:           _Z5ln2_kPKDF16_PKfS2_Pf
    .private_segment_fixed_size: 0
    .sgpr_count:     18
    .sgpr_spill_count: 0
    .symbol:         _Z5ln2_kPKDF16_PKfS2_Pf.kd
    .uniform_work_group_size: 1
    .uses_dynamic_stack: false
    .vgpr_count:     37
    .vgpr_spill_count: 0
    .wavefront_size: 64
  - .agpr_count:     256
    .args:
      - .address_space:  global
        .offset:         0
        .size:           8
        .value_kind:     global_buffer
      - .address_space:  global
        .offset:         8
        .size:           8
        .value_kind:     global_buffer
      - .offset:         16
        .size:           4
        .value_kind:     by_value
      - .offset:         20
        .size:           4
        .value_kind:     by_value
      - .offset:         24
        .size:           4
        .value_kind:     by_value
      - .actual_access:  read_only
        .address_space:  global
        .offset:         32
        .size:           8
        .value_kind:     global_buffer
      - .actual_access:  read_only
        .address_space:  global
        .offset:         40
        .size:           8
        .value_kind:     global_buffer
      - .actual_access:  write_only
        .address_space:  global
        .offset:         48
        .size:           8
        .value_kind:     global_buffer
      - .actual_access:  read_only
        .address_space:  global
        .offset:         56
        .size:           8
        .value_kind:     global_buffer
      - .actual_access:  write_only
        .address_space:  global
        .offset:         64
        .size:           8
        .value_kind:     global_buffer
    .group_segment_fixed_size: 81920
    .kernarg_segment_align: 8
    .kernarg_segment_size: 72
    .language:       OpenCL C
    .language_version:
      - 2
      - 0
    .max_flat_workgroup_size: 256
    .name:           _Z6gemm_kILi0ELi1ELi2EEvPKDF16_S1_iiiPKfS1_PDF16_PfS4_
    .private_segment_fixed_size: 0
    .sgpr_count:     70
    .sgpr_spill_count: 0
    .symbol:         _Z6gemm_kILi0ELi1ELi2EEvPKDF16_S1_iiiPKfS1_PDF16_PfS4_.kd
    .uniform_work_group_size: 1
    .uses_dynamic_stack: false
    .vgpr_count:     512
    .vgpr_spill_count: 0
    .wavefront_size: 64
  - .agpr_count:     256
    .args:
      - .address_space:  global
        .offset:         0
        .size:           8
        .value_kind:     global_buffer
      - .address_space:  global
        .offset:         8
        .size:           8
        .value_kind:     global_buffer
      - .offset:         16
        .size:           4
        .value_kind:     by_value
      - .offset:         20
        .size:           4
        .value_kind:     by_value
      - .offset:         24
        .size:           4
        .value_kind:     by_value
      - .actual_access:  read_only
        .address_space:  global
        .offset:         32
        .size:           8
        .value_kind:     global_buffer
      - .actual_access:  read_only
        .address_space:  global
        .offset:         40
        .size:           8
        .value_kind:     global_buffer
      - .actual_access:  write_only
        .address_space:  global
        .offset:         48
        .size:           8
        .value_kind:     global_buffer
      - .actual_access:  read_only
        .address_space:  global
        .offset:         56
        .size:           8
        .value_kind:     global_buffer
      - .actual_access:  read_only
        .address_space:  global
        .offset:         64
        .size:           8
        .value_kind:     global_buffer
    .group_segment_fixed_size: 81920
    .kernarg_segment_align: 8
    .kernarg_segment_size: 72
    .language:       OpenCL C
    .language_version:
      - 2
      - 0
    .max_flat_workgroup_size: 256
    .name:           _Z6gemm_kILi1ELi2ELi2EEvPKDF16_S1_iiiPKfS1_PDF16_PfS4_
    .private_segment_fixed_size: 0
    .sgpr_count:     62
    .sgpr_spill_count: 0
    .symbol:         _Z6gemm_kILi1ELi2ELi2EEvPKDF16_S1_iiiPKfS1_PDF16_PfS4_.kd
    .uniform_work_group_size: 1
    .uses_dynamic_stack: false
    .vgpr_count:     512
    .vgpr_spill_count: 0
    .wavefront_size: 64
  - .agpr_count:     256
    .args:
      - .address_space:  global
        .offset:         0
        .size:           8
        .value_kind:     global_buffer
      - .address_space:  global
        .offset:         8
        .size:           8
        .value_kind:     global_buffer
      - .offset:         16
        .size:           4
        .value_kind:     by_value
      - .offset:         20
        .size:           4
        .value_kind:     by_value
      - .offset:         24
        .size:           4
        .value_kind:     by_value
      - .actual_access:  read_only
        .address_space:  global
        .offset:         32
        .size:           8
        .value_kind:     global_buffer
      - .actual_access:  read_only
        .address_space:  global
        .offset:         40
        .size:           8
        .value_kind:     global_buffer
      - .actual_access:  write_only
        .address_space:  global
        .offset:         48
        .size:           8
        .value_kind:     global_buffer
      - .actual_access:  read_only
        .address_space:  global
        .offset:         56
        .size:           8
        .value_kind:     global_buffer
      - .actual_access:  read_only
        .address_space:  global
        .offset:         64
        .size:           8
        .value_kind:     global_buffer
    .group_segment_fixed_size: 131072
    .kernarg_segment_align: 8
    .kernarg_segment_size: 72
    .language:       OpenCL C
    .language_version:
      - 2
      - 0
    .max_flat_workgroup_size: 256
    .name:           _Z6gemm_kILi2ELi3ELi2EEvPKDF16_S1_iiiPKfS1_PDF16_PfS4_
    .private_segment_fixed_size: 0
    .sgpr_count:     54
    .sgpr_spill_count: 0
    .symbol:         _Z6gemm_kILi2ELi3ELi2EEvPKDF16_S1_iiiPKfS1_PDF16_PfS4_.kd
    .uniform_work_group_size: 1
    .uses_dynamic_stack: false
    .vgpr_count:     512
    .vgpr_spill_count: 0
    .wavefront_size: 64
